# P1 in_proj epilogue (roped k tiles): rope-table reads of the 8 row blocks double-buffered in dead fragment registers instead of load->vmcnt(0) per block
# baseline (speedup 1.0000x reference)
.LBB0_321:
	v_mov_b64_e32 v[140:141], v[116:117]
	v_mov_b64_e32 v[136:137], v[120:121]
	v_mov_b64_e32 v[144:145], v[124:125]
	v_mov_b64_e32 v[132:133], v[128:129]
	v_and_b32_e32 v179, 0x7cf, v178
	s_andn2_b64 vcc, exec, s[4:5]
	v_mov_b64_e32 v[138:139], v[114:115]
	v_mov_b64_e32 v[134:135], v[118:119]
	v_mov_b64_e32 v[142:143], v[122:123]
	v_mov_b64_e32 v[130:131], v[126:127]
	s_cbranch_vccnz .LBB0_323
	v_lshlrev_b32_e32 v158, 9, v179
	v_lshl_add_u64 v[130:131], v[168:169], 0, v[158:159]
	v_mov_b32_e32 v254, v178
	v_and_b32_e32 v254, 0x7ff, v254
	v_lshlrev_b32_e32 v254, 9, v254
	v_mov_b32_e32 v255, 0
	v_lshl_add_u64 v[254:255], v[168:169], 0, v[254:255]
	global_load_dwordx4 v[198:201], v[254:255], off
	global_load_dwordx4 v[202:205], v[254:255], off offset:16
	global_load_dwordx4 v[206:209], v[254:255], off offset:32
	global_load_dwordx4 v[210:213], v[254:255], off offset:48
	v_add_u32_e32 v254, 0x10, v178
	v_and_b32_e32 v254, 0x7ff, v254
	v_lshlrev_b32_e32 v254, 9, v254
	v_mov_b32_e32 v255, 0
	v_lshl_add_u64 v[254:255], v[168:169], 0, v[254:255]
	global_load_dwordx4 v[214:217], v[254:255], off
	global_load_dwordx4 v[218:221], v[254:255], off offset:16
	global_load_dwordx4 v[222:225], v[254:255], off offset:32
	global_load_dwordx4 v[230:233], v[254:255], off offset:48
	s_waitcnt vmcnt(4)
	v_mov_b32_e32 v138, v210
	v_mov_b32_e32 v139, v211
	v_mov_b32_e32 v140, v212
	v_mov_b32_e32 v141, v213
	v_mov_b32_e32 v142, v206
	v_mov_b32_e32 v143, v207
	v_mov_b32_e32 v144, v208
	v_mov_b32_e32 v145, v209
	v_mov_b32_e32 v132, v202
	v_mov_b32_e32 v133, v203
	v_mov_b32_e32 v134, v204
	v_mov_b32_e32 v135, v205
	v_mov_b32_e32 v180, v198
	v_mov_b32_e32 v181, v199
	v_mov_b32_e32 v182, v200
	v_mov_b32_e32 v183, v201
	v_add_u32_e32 v254, 0x20, v178
	v_and_b32_e32 v254, 0x7ff, v254
	v_lshlrev_b32_e32 v254, 9, v254
	v_mov_b32_e32 v255, 0
	v_lshl_add_u64 v[254:255], v[168:169], 0, v[254:255]
	global_load_dwordx4 v[198:201], v[254:255], off
	global_load_dwordx4 v[202:205], v[254:255], off offset:16
	global_load_dwordx4 v[206:209], v[254:255], off offset:32
	global_load_dwordx4 v[210:213], v[254:255], off offset:48
	v_mul_f32_e32 v184, v120, v133
	v_mov_b32_e32 v137, v182
	v_mov_b32_e32 v182, v181
	v_mov_b32_e32 v136, v180
	v_pk_mul_f32 v[130:131], v[118:119], v[182:183]
	v_pk_mul_f32 v[180:181], v[126:127], v[182:183]
	v_mul_f32_e32 v182, v128, v132
	v_mul_f32_e32 v186, v120, v132
	v_mul_f32_e32 v190, v128, v133
	v_mov_b32_e32 v132, v129
	v_mov_b32_e32 v133, v121
	v_pk_mul_f32 v[132:133], v[132:133], v[134:135]
	v_pk_fma_f32 v[130:131], v[126:127], v[136:137], v[130:131] neg_lo:[0,0,1] neg_hi:[0,0,1]
	v_mov_b32_e32 v183, v132
	v_mov_b32_e32 v185, v133
	v_pk_add_f32 v[132:133], v[182:183], v[184:185] neg_lo:[0,1] neg_hi:[0,1]
	v_mov_b32_e32 v182, v121
	v_mov_b32_e32 v183, v129
	v_pk_mul_f32 v[134:135], v[182:183], v[134:135]
	v_mul_f32_e32 v184, v116, v139
	v_mov_b32_e32 v187, v134
	v_mov_b32_e32 v191, v135
	v_pk_fma_f32 v[134:135], v[118:119], v[136:137], v[180:181]
	v_mov_b32_e32 v181, v144
	v_mov_b32_e32 v144, v143
	v_pk_add_f32 v[136:137], v[186:187], v[190:191]
	v_mov_b32_e32 v180, v142
	v_pk_mul_f32 v[142:143], v[114:115], v[144:145]
	v_pk_mul_f32 v[182:183], v[122:123], v[144:145]
	v_mul_f32_e32 v144, v124, v138
	v_mul_f32_e32 v186, v116, v138
	v_mul_f32_e32 v190, v124, v139
	v_mov_b32_e32 v138, v125
	v_mov_b32_e32 v139, v117
	v_pk_mul_f32 v[138:139], v[138:139], v[140:141]
	v_pk_fma_f32 v[142:143], v[122:123], v[180:181], v[142:143] neg_lo:[0,0,1] neg_hi:[0,0,1]
	v_mov_b32_e32 v145, v138
	v_mov_b32_e32 v185, v139
	v_mov_b32_e32 v138, v117
	v_mov_b32_e32 v139, v125
	v_pk_mul_f32 v[138:139], v[138:139], v[140:141]
	v_pk_add_f32 v[144:145], v[144:145], v[184:185] neg_lo:[0,1] neg_hi:[0,1]
	v_mov_b32_e32 v187, v138
	v_mov_b32_e32 v191, v139
	v_pk_fma_f32 v[138:139], v[114:115], v[180:181], v[182:183]
	v_pk_add_f32 v[140:141], v[186:187], v[190:191]

.LBB0_331:
	s_movk_i32 s33, 0x7df
	v_mov_b64_e32 v[124:125], v[100:101]
	v_mov_b64_e32 v[120:121], v[104:105]
	v_mov_b64_e32 v[128:129], v[108:109]
	v_mov_b64_e32 v[116:117], v[112:113]
	v_bitop3_b32 v132, v178, s33, 16 bitop3:0xc8
	s_andn2_b64 vcc, exec, s[8:9]
	v_mov_b64_e32 v[122:123], v[98:99]
	v_mov_b64_e32 v[118:119], v[102:103]
	v_mov_b64_e32 v[126:127], v[106:107]
	v_mov_b64_e32 v[114:115], v[110:111]
	s_cbranch_vccnz .LBB0_333
	v_lshlrev_b32_e32 v114, 9, v132
	v_mov_b32_e32 v115, v159
	v_lshl_add_u64 v[114:115], v[168:169], 0, v[114:115]
	s_waitcnt vmcnt(6)
	v_mov_b32_e32 v122, v230
	v_mov_b32_e32 v123, v231
	v_mov_b32_e32 v124, v232
	v_mov_b32_e32 v125, v233
	v_mov_b32_e32 v126, v222
	v_mov_b32_e32 v127, v223
	v_mov_b32_e32 v128, v224
	v_mov_b32_e32 v129, v225
	v_mov_b32_e32 v116, v218
	v_mov_b32_e32 v117, v219
	v_mov_b32_e32 v118, v220
	v_mov_b32_e32 v119, v221
	v_mov_b32_e32 v134, v214
	v_mov_b32_e32 v135, v215
	v_mov_b32_e32 v136, v216
	v_mov_b32_e32 v137, v217
	v_add_u32_e32 v254, 0x30, v178
	v_and_b32_e32 v254, 0x7ff, v254
	v_lshlrev_b32_e32 v254, 9, v254
	v_mov_b32_e32 v255, 0
	v_lshl_add_u64 v[254:255], v[168:169], 0, v[254:255]
	global_load_dwordx4 v[214:217], v[254:255], off
	global_load_dwordx4 v[218:221], v[254:255], off offset:16
	global_load_dwordx4 v[222:225], v[254:255], off offset:32
	global_load_dwordx4 v[230:233], v[254:255], off offset:48
	v_mul_f32_e32 v138, v104, v116
	v_mov_b32_e32 v121, v136
	v_mov_b32_e32 v136, v135
	v_mov_b32_e32 v120, v134
	v_pk_mul_f32 v[114:115], v[102:103], v[136:137]
	v_pk_mul_f32 v[130:131], v[110:111], v[136:137]
	v_mul_f32_e32 v134, v112, v116
	v_mul_f32_e32 v136, v104, v117
	v_mul_f32_e32 v140, v112, v117
	v_mov_b32_e32 v116, v113
	v_mov_b32_e32 v117, v105
	v_pk_mul_f32 v[116:117], v[116:117], v[118:119]
	v_pk_fma_f32 v[114:115], v[110:111], v[120:121], v[114:115] neg_lo:[0,0,1] neg_hi:[0,0,1]
	v_mov_b32_e32 v135, v116
	v_mov_b32_e32 v137, v117
	v_pk_add_f32 v[116:117], v[134:135], v[136:137] neg_lo:[0,1] neg_hi:[0,1]
	v_mov_b32_e32 v134, v105
	v_mov_b32_e32 v135, v113
	v_pk_mul_f32 v[118:119], v[134:135], v[118:119]
	v_mul_f32_e32 v136, v100, v123
	v_mov_b32_e32 v139, v118
	v_mov_b32_e32 v141, v119
	v_pk_fma_f32 v[118:119], v[102:103], v[120:121], v[130:131]
	v_mov_b32_e32 v131, v128
	v_mov_b32_e32 v128, v127
	v_pk_add_f32 v[120:121], v[138:139], v[140:141]
	v_mov_b32_e32 v130, v126
	v_pk_mul_f32 v[126:127], v[98:99], v[128:129]
	v_pk_mul_f32 v[134:135], v[106:107], v[128:129]
	v_mul_f32_e32 v128, v108, v122
	v_mul_f32_e32 v138, v100, v122
	v_mul_f32_e32 v140, v108, v123
	v_mov_b32_e32 v122, v109
	v_mov_b32_e32 v123, v101
	v_pk_mul_f32 v[122:123], v[122:123], v[124:125]
	v_pk_fma_f32 v[126:127], v[106:107], v[130:131], v[126:127] neg_lo:[0,0,1] neg_hi:[0,0,1]
	v_mov_b32_e32 v129, v122
	v_mov_b32_e32 v137, v123
	v_mov_b32_e32 v122, v101
	v_mov_b32_e32 v123, v109
	v_pk_mul_f32 v[122:123], v[122:123], v[124:125]
	v_pk_add_f32 v[128:129], v[128:129], v[136:137] neg_lo:[0,1] neg_hi:[0,1]
	v_mov_b32_e32 v139, v122
	v_mov_b32_e32 v141, v123
	v_pk_fma_f32 v[122:123], v[98:99], v[130:131], v[134:135]
	v_pk_add_f32 v[124:125], v[138:139], v[140:141]

.LBB0_341:
	s_movk_i32 s33, 0x7ef
	v_mov_b64_e32 v[108:109], v[84:85]
	v_mov_b64_e32 v[104:105], v[88:89]
	v_mov_b64_e32 v[112:113], v[92:93]
	v_mov_b64_e32 v[100:101], v[96:97]
	v_bitop3_b32 v116, v178, s33, 32 bitop3:0xc8
	s_andn2_b64 vcc, exec, s[52:53]
	v_mov_b64_e32 v[106:107], v[82:83]
	v_mov_b64_e32 v[102:103], v[86:87]
	v_mov_b64_e32 v[110:111], v[90:91]
	v_mov_b64_e32 v[98:99], v[94:95]
	s_cbranch_vccnz .LBB0_347
	v_lshlrev_b32_e32 v98, 9, v116
	v_mov_b32_e32 v99, v159
	v_lshl_add_u64 v[98:99], v[168:169], 0, v[98:99]
	s_waitcnt vmcnt(8)
	v_mov_b32_e32 v106, v210
	v_mov_b32_e32 v107, v211
	v_mov_b32_e32 v108, v212
	v_mov_b32_e32 v109, v213
	v_mov_b32_e32 v110, v206
	v_mov_b32_e32 v111, v207
	v_mov_b32_e32 v112, v208
	v_mov_b32_e32 v113, v209
	v_mov_b32_e32 v100, v202
	v_mov_b32_e32 v101, v203
	v_mov_b32_e32 v102, v204
	v_mov_b32_e32 v103, v205
	v_mov_b32_e32 v118, v198
	v_mov_b32_e32 v119, v199
	v_mov_b32_e32 v120, v200
	v_mov_b32_e32 v121, v201
	v_add_u32_e32 v254, 0x80, v178
	v_and_b32_e32 v254, 0x7ff, v254
	v_lshlrev_b32_e32 v254, 9, v254
	v_mov_b32_e32 v255, 0
	v_lshl_add_u64 v[254:255], v[168:169], 0, v[254:255]
	global_load_dwordx4 v[198:201], v[254:255], off
	global_load_dwordx4 v[202:205], v[254:255], off offset:16
	global_load_dwordx4 v[206:209], v[254:255], off offset:32
	global_load_dwordx4 v[210:213], v[254:255], off offset:48
	v_mul_f32_e32 v122, v88, v100
	v_mov_b32_e32 v105, v120
	v_mov_b32_e32 v120, v119
	v_mov_b32_e32 v104, v118
	v_pk_mul_f32 v[98:99], v[86:87], v[120:121]
	v_pk_mul_f32 v[114:115], v[94:95], v[120:121]
	v_mul_f32_e32 v118, v96, v100
	v_mul_f32_e32 v120, v88, v101
	v_mul_f32_e32 v124, v96, v101
	v_mov_b32_e32 v100, v97
	v_mov_b32_e32 v101, v89
	v_pk_mul_f32 v[100:101], v[100:101], v[102:103]
	v_pk_fma_f32 v[98:99], v[94:95], v[104:105], v[98:99] neg_lo:[0,0,1] neg_hi:[0,0,1]
	v_mov_b32_e32 v119, v100
	v_mov_b32_e32 v121, v101
	v_pk_add_f32 v[100:101], v[118:119], v[120:121] neg_lo:[0,1] neg_hi:[0,1]
	v_mov_b32_e32 v118, v89
	v_mov_b32_e32 v119, v97
	v_pk_mul_f32 v[102:103], v[118:119], v[102:103]
	v_mul_f32_e32 v120, v84, v107
	v_mov_b32_e32 v123, v102
	v_mov_b32_e32 v125, v103
	v_pk_fma_f32 v[102:103], v[86:87], v[104:105], v[114:115]
	v_mov_b32_e32 v115, v112
	v_mov_b32_e32 v112, v111
	v_pk_add_f32 v[104:105], v[122:123], v[124:125]
	v_mov_b32_e32 v114, v110
	v_pk_mul_f32 v[110:111], v[82:83], v[112:113]
	v_pk_mul_f32 v[118:119], v[90:91], v[112:113]
	v_mul_f32_e32 v112, v92, v106
	v_mul_f32_e32 v122, v84, v106
	v_mul_f32_e32 v124, v92, v107
	v_mov_b32_e32 v106, v93
	v_mov_b32_e32 v107, v85
	v_pk_mul_f32 v[106:107], v[106:107], v[108:109]
	v_pk_fma_f32 v[110:111], v[90:91], v[114:115], v[110:111] neg_lo:[0,0,1] neg_hi:[0,0,1]
	v_mov_b32_e32 v113, v106
	v_mov_b32_e32 v121, v107
	v_mov_b32_e32 v106, v85
	v_mov_b32_e32 v107, v93
	v_pk_mul_f32 v[106:107], v[106:107], v[108:109]
	v_pk_add_f32 v[112:113], v[112:113], v[120:121] neg_lo:[0,1] neg_hi:[0,1]
	v_mov_b32_e32 v123, v106
	v_mov_b32_e32 v125, v107
	v_pk_fma_f32 v[106:107], v[82:83], v[114:115], v[118:119]
	v_pk_add_f32 v[108:109], v[122:123], v[124:125]
	s_and_b64 vcc, exec, s[8:9]
	s_mov_b64 s[52:53], -1
	s_cbranch_vccz .LBB0_348

.LBB0_351:
	s_movk_i32 s33, 0x7ff
	v_mov_b64_e32 v[92:93], v[68:69]
	v_mov_b64_e32 v[88:89], v[72:73]
	v_mov_b64_e32 v[96:97], v[76:77]
	v_mov_b64_e32 v[84:85], v[80:81]
	v_bitop3_b32 v100, v178, s33, 48 bitop3:0xc8
	s_andn2_b64 vcc, exec, s[52:53]
	v_mov_b64_e32 v[90:91], v[66:67]
	v_mov_b64_e32 v[86:87], v[70:71]
	v_mov_b64_e32 v[94:95], v[74:75]
	v_mov_b64_e32 v[82:83], v[78:79]
	s_cbranch_vccnz .LBB0_357
	v_lshlrev_b32_e32 v82, 9, v100
	v_mov_b32_e32 v83, v159
	v_lshl_add_u64 v[82:83], v[168:169], 0, v[82:83]
	s_waitcnt vmcnt(8)
	v_mov_b32_e32 v90, v230
	v_mov_b32_e32 v91, v231
	v_mov_b32_e32 v92, v232
	v_mov_b32_e32 v93, v233
	v_mov_b32_e32 v94, v222
	v_mov_b32_e32 v95, v223
	v_mov_b32_e32 v96, v224
	v_mov_b32_e32 v97, v225
	v_mov_b32_e32 v84, v218
	v_mov_b32_e32 v85, v219
	v_mov_b32_e32 v86, v220
	v_mov_b32_e32 v87, v221
	v_mov_b32_e32 v102, v214
	v_mov_b32_e32 v103, v215
	v_mov_b32_e32 v104, v216
	v_mov_b32_e32 v105, v217
	v_add_u32_e32 v254, 0x90, v178
	v_and_b32_e32 v254, 0x7ff, v254
	v_lshlrev_b32_e32 v254, 9, v254
	v_mov_b32_e32 v255, 0
	v_lshl_add_u64 v[254:255], v[168:169], 0, v[254:255]
	global_load_dwordx4 v[214:217], v[254:255], off
	global_load_dwordx4 v[218:221], v[254:255], off offset:16
	global_load_dwordx4 v[222:225], v[254:255], off offset:32
	global_load_dwordx4 v[230:233], v[254:255], off offset:48
	v_mul_f32_e32 v106, v72, v84
	v_mov_b32_e32 v89, v104
	v_mov_b32_e32 v104, v103
	v_mov_b32_e32 v88, v102
	v_pk_mul_f32 v[82:83], v[70:71], v[104:105]
	v_pk_mul_f32 v[98:99], v[78:79], v[104:105]
	v_mul_f32_e32 v102, v80, v84
	v_mul_f32_e32 v104, v72, v85
	v_mul_f32_e32 v108, v80, v85
	v_mov_b32_e32 v84, v81
	v_mov_b32_e32 v85, v73
	v_pk_mul_f32 v[84:85], v[84:85], v[86:87]
	v_pk_fma_f32 v[82:83], v[78:79], v[88:89], v[82:83] neg_lo:[0,0,1] neg_hi:[0,0,1]
	v_mov_b32_e32 v103, v84
	v_mov_b32_e32 v105, v85
	v_pk_add_f32 v[84:85], v[102:103], v[104:105] neg_lo:[0,1] neg_hi:[0,1]
	v_mov_b32_e32 v102, v73
	v_mov_b32_e32 v103, v81
	v_pk_mul_f32 v[86:87], v[102:103], v[86:87]
	v_mul_f32_e32 v104, v68, v91
	v_mov_b32_e32 v107, v86
	v_mov_b32_e32 v109, v87
	v_pk_fma_f32 v[86:87], v[70:71], v[88:89], v[98:99]
	v_mov_b32_e32 v99, v96
	v_mov_b32_e32 v96, v95
	v_pk_add_f32 v[88:89], v[106:107], v[108:109]
	v_mov_b32_e32 v98, v94
	v_pk_mul_f32 v[94:95], v[66:67], v[96:97]
	v_pk_mul_f32 v[102:103], v[74:75], v[96:97]
	v_mul_f32_e32 v96, v76, v90
	v_mul_f32_e32 v106, v68, v90
	v_mul_f32_e32 v108, v76, v91
	v_mov_b32_e32 v90, v77
	v_mov_b32_e32 v91, v69
	v_pk_mul_f32 v[90:91], v[90:91], v[92:93]
	v_pk_fma_f32 v[94:95], v[74:75], v[98:99], v[94:95] neg_lo:[0,0,1] neg_hi:[0,0,1]
	v_mov_b32_e32 v97, v90
	v_mov_b32_e32 v105, v91
	v_mov_b32_e32 v90, v69
	v_mov_b32_e32 v91, v77
	v_pk_mul_f32 v[90:91], v[90:91], v[92:93]
	v_pk_add_f32 v[96:97], v[96:97], v[104:105] neg_lo:[0,1] neg_hi:[0,1]
	v_mov_b32_e32 v107, v90
	v_mov_b32_e32 v109, v91
	v_pk_fma_f32 v[90:91], v[66:67], v[98:99], v[102:103]
	v_pk_add_f32 v[92:93], v[106:107], v[108:109]
	s_and_b64 vcc, exec, s[8:9]
	s_mov_b64 s[52:53], -1
	s_cbranch_vccz .LBB0_358

.LBB0_361:
	v_add_u32_e32 v82, 0x80, v178
	v_mov_b64_e32 v[76:77], v[64:65]
	v_mov_b64_e32 v[72:73], v[60:61]
	v_mov_b64_e32 v[80:81], v[52:53]
	v_mov_b64_e32 v[68:69], v[56:57]
	v_and_b32_e32 v83, 0x7cf, v82
	s_andn2_b64 vcc, exec, s[52:53]
	v_mov_b64_e32 v[74:75], v[62:63]
	v_mov_b64_e32 v[70:71], v[58:59]
	v_mov_b64_e32 v[78:79], v[50:51]
	v_mov_b64_e32 v[66:67], v[54:55]
	s_cbranch_vccnz .LBB0_363
	v_lshlrev_b32_e32 v66, 9, v83
	v_mov_b32_e32 v67, v159
	v_lshl_add_u64 v[66:67], v[168:169], 0, v[66:67]
	s_waitcnt vmcnt(8)
	v_mov_b32_e32 v74, v210
	v_mov_b32_e32 v75, v211
	v_mov_b32_e32 v76, v212
	v_mov_b32_e32 v77, v213
	v_mov_b32_e32 v78, v206
	v_mov_b32_e32 v79, v207
	v_mov_b32_e32 v80, v208
	v_mov_b32_e32 v81, v209
	v_mov_b32_e32 v68, v202
	v_mov_b32_e32 v69, v203
	v_mov_b32_e32 v70, v204
	v_mov_b32_e32 v71, v205
	v_mov_b32_e32 v84, v198
	v_mov_b32_e32 v85, v199
	v_mov_b32_e32 v86, v200
	v_mov_b32_e32 v87, v201
	v_add_u32_e32 v254, 0xa0, v178
	v_and_b32_e32 v254, 0x7ff, v254
	v_lshlrev_b32_e32 v254, 9, v254
	v_mov_b32_e32 v255, 0
	v_lshl_add_u64 v[254:255], v[168:169], 0, v[254:255]
	global_load_dwordx4 v[198:201], v[254:255], off
	global_load_dwordx4 v[202:205], v[254:255], off offset:16
	global_load_dwordx4 v[206:209], v[254:255], off offset:32
	global_load_dwordx4 v[210:213], v[254:255], off offset:48
	v_mul_f32_e32 v88, v60, v69
	v_mov_b32_e32 v73, v86
	v_mov_b32_e32 v86, v85
	v_mov_b32_e32 v72, v84
	v_pk_mul_f32 v[66:67], v[58:59], v[86:87]
	v_pk_mul_f32 v[84:85], v[54:55], v[86:87]
	v_mul_f32_e32 v86, v56, v68
	v_mul_f32_e32 v90, v60, v68
	v_mul_f32_e32 v92, v56, v69
	v_mov_b32_e32 v68, v57
	v_mov_b32_e32 v69, v61
	v_pk_mul_f32 v[68:69], v[68:69], v[70:71]
	v_pk_fma_f32 v[66:67], v[54:55], v[72:73], v[66:67] neg_lo:[0,0,1] neg_hi:[0,0,1]
	v_mov_b32_e32 v87, v68
	v_mov_b32_e32 v89, v69
	v_pk_add_f32 v[68:69], v[86:87], v[88:89] neg_lo:[0,1] neg_hi:[0,1]
	v_mov_b32_e32 v86, v61
	v_mov_b32_e32 v87, v57
	v_pk_mul_f32 v[70:71], v[86:87], v[70:71]
	v_mul_f32_e32 v88, v64, v75
	v_mov_b32_e32 v91, v70
	v_mov_b32_e32 v93, v71
	v_pk_fma_f32 v[70:71], v[58:59], v[72:73], v[84:85]
	v_mov_b32_e32 v85, v80
	v_mov_b32_e32 v80, v79
	v_pk_add_f32 v[72:73], v[90:91], v[92:93]
	v_mov_b32_e32 v84, v78
	v_pk_mul_f32 v[78:79], v[62:63], v[80:81]
	v_pk_mul_f32 v[86:87], v[50:51], v[80:81]
	v_mul_f32_e32 v80, v52, v74
	v_mul_f32_e32 v90, v64, v74
	v_mul_f32_e32 v92, v52, v75
	v_mov_b32_e32 v74, v53
	v_mov_b32_e32 v75, v65
	v_pk_mul_f32 v[74:75], v[74:75], v[76:77]
	v_pk_fma_f32 v[78:79], v[50:51], v[84:85], v[78:79] neg_lo:[0,0,1] neg_hi:[0,0,1]
	v_mov_b32_e32 v81, v74
	v_mov_b32_e32 v89, v75
	v_mov_b32_e32 v74, v65
	v_mov_b32_e32 v75, v53
	v_pk_mul_f32 v[74:75], v[74:75], v[76:77]
	v_pk_add_f32 v[80:81], v[80:81], v[88:89] neg_lo:[0,1] neg_hi:[0,1]
	v_mov_b32_e32 v91, v74
	v_mov_b32_e32 v93, v75
	v_pk_fma_f32 v[74:75], v[62:63], v[84:85], v[86:87]
	v_pk_add_f32 v[76:77], v[90:91], v[92:93]

.LBB0_371:
	v_add_u32_e32 v66, 0x90, v178
	v_mov_b64_e32 v[60:61], v[48:49]
	v_mov_b64_e32 v[56:57], v[44:45]
	v_mov_b64_e32 v[64:65], v[36:37]
	v_mov_b64_e32 v[52:53], v[40:41]
	v_and_b32_e32 v67, 0x7df, v66
	s_andn2_b64 vcc, exec, s[52:53]
	v_mov_b64_e32 v[58:59], v[46:47]
	v_mov_b64_e32 v[54:55], v[42:43]
	v_mov_b64_e32 v[62:63], v[34:35]
	v_mov_b64_e32 v[50:51], v[38:39]
	s_cbranch_vccnz .LBB0_377
	v_lshlrev_b32_e32 v50, 9, v67
	v_mov_b32_e32 v51, v159
	v_lshl_add_u64 v[50:51], v[168:169], 0, v[50:51]
	s_waitcnt vmcnt(8)
	v_mov_b32_e32 v58, v230
	v_mov_b32_e32 v59, v231
	v_mov_b32_e32 v60, v232
	v_mov_b32_e32 v61, v233
	v_mov_b32_e32 v62, v222
	v_mov_b32_e32 v63, v223
	v_mov_b32_e32 v64, v224
	v_mov_b32_e32 v65, v225
	v_mov_b32_e32 v52, v218
	v_mov_b32_e32 v53, v219
	v_mov_b32_e32 v54, v220
	v_mov_b32_e32 v55, v221
	v_mov_b32_e32 v68, v214
	v_mov_b32_e32 v69, v215
	v_mov_b32_e32 v70, v216
	v_mov_b32_e32 v71, v217
	v_add_u32_e32 v254, 0xb0, v178
	v_and_b32_e32 v254, 0x7ff, v254
	v_lshlrev_b32_e32 v254, 9, v254
	v_mov_b32_e32 v255, 0
	v_lshl_add_u64 v[254:255], v[168:169], 0, v[254:255]
	global_load_dwordx4 v[214:217], v[254:255], off
	global_load_dwordx4 v[218:221], v[254:255], off offset:16
	global_load_dwordx4 v[222:225], v[254:255], off offset:32
	global_load_dwordx4 v[230:233], v[254:255], off offset:48
	v_mul_f32_e32 v72, v44, v53
	v_mov_b32_e32 v57, v70
	v_mov_b32_e32 v70, v69
	v_mov_b32_e32 v56, v68
	v_pk_mul_f32 v[50:51], v[42:43], v[70:71]
	v_pk_mul_f32 v[68:69], v[38:39], v[70:71]
	v_mul_f32_e32 v70, v40, v52
	v_mul_f32_e32 v74, v44, v52
	v_mul_f32_e32 v76, v40, v53
	v_mov_b32_e32 v52, v41
	v_mov_b32_e32 v53, v45
	v_pk_mul_f32 v[52:53], v[52:53], v[54:55]
	v_pk_fma_f32 v[50:51], v[38:39], v[56:57], v[50:51] neg_lo:[0,0,1] neg_hi:[0,0,1]
	v_mov_b32_e32 v71, v52
	v_mov_b32_e32 v73, v53
	v_pk_add_f32 v[52:53], v[70:71], v[72:73] neg_lo:[0,1] neg_hi:[0,1]
	v_mov_b32_e32 v70, v45
	v_mov_b32_e32 v71, v41
	v_pk_mul_f32 v[54:55], v[70:71], v[54:55]
	v_mul_f32_e32 v72, v48, v59
	v_mov_b32_e32 v75, v54
	v_mov_b32_e32 v77, v55
	v_pk_fma_f32 v[54:55], v[42:43], v[56:57], v[68:69]
	v_mov_b32_e32 v69, v64
	v_mov_b32_e32 v64, v63
	v_pk_add_f32 v[56:57], v[74:75], v[76:77]
	v_mov_b32_e32 v68, v62
	v_pk_mul_f32 v[62:63], v[46:47], v[64:65]
	v_pk_mul_f32 v[70:71], v[34:35], v[64:65]
	v_mul_f32_e32 v64, v36, v58
	v_mul_f32_e32 v74, v48, v58
	v_mul_f32_e32 v76, v36, v59
	v_mov_b32_e32 v58, v37
	v_mov_b32_e32 v59, v49
	v_pk_mul_f32 v[58:59], v[58:59], v[60:61]
	v_pk_fma_f32 v[62:63], v[34:35], v[68:69], v[62:63] neg_lo:[0,0,1] neg_hi:[0,0,1]
	v_mov_b32_e32 v65, v58
	v_mov_b32_e32 v73, v59
	v_mov_b32_e32 v58, v49
	v_mov_b32_e32 v59, v37
	v_pk_mul_f32 v[58:59], v[58:59], v[60:61]
	v_pk_add_f32 v[64:65], v[64:65], v[72:73] neg_lo:[0,1] neg_hi:[0,1]
	v_mov_b32_e32 v75, v58
	v_mov_b32_e32 v77, v59
	v_pk_fma_f32 v[58:59], v[46:47], v[68:69], v[70:71]
	v_pk_add_f32 v[60:61], v[74:75], v[76:77]
	s_and_b64 vcc, exec, s[8:9]
	s_mov_b64 s[52:53], -1
	s_cbranch_vccz .LBB0_378

.LBB0_381:
	v_add_u32_e32 v50, 0xa0, v178
	v_mov_b64_e32 v[44:45], v[32:33]
	v_mov_b64_e32 v[40:41], v[28:29]
	v_mov_b64_e32 v[48:49], v[20:21]
	v_mov_b64_e32 v[36:37], v[24:25]
	v_and_b32_e32 v51, 0x7ef, v50
	s_andn2_b64 vcc, exec, s[52:53]
	v_mov_b64_e32 v[42:43], v[30:31]
	v_mov_b64_e32 v[38:39], v[26:27]
	v_mov_b64_e32 v[46:47], v[18:19]
	v_mov_b64_e32 v[34:35], v[22:23]
	s_cbranch_vccnz .LBB0_387
	v_lshlrev_b32_e32 v34, 9, v51
	v_mov_b32_e32 v35, v159
	v_lshl_add_u64 v[34:35], v[168:169], 0, v[34:35]
	s_waitcnt vmcnt(8)
	v_mov_b32_e32 v42, v210
	v_mov_b32_e32 v43, v211
	v_mov_b32_e32 v44, v212
	v_mov_b32_e32 v45, v213
	v_mov_b32_e32 v46, v206
	v_mov_b32_e32 v47, v207
	v_mov_b32_e32 v48, v208
	v_mov_b32_e32 v49, v209
	v_mov_b32_e32 v36, v202
	v_mov_b32_e32 v37, v203
	v_mov_b32_e32 v38, v204
	v_mov_b32_e32 v39, v205
	v_mov_b32_e32 v52, v198
	v_mov_b32_e32 v53, v199
	v_mov_b32_e32 v54, v200
	v_mov_b32_e32 v55, v201
	v_mul_f32_e32 v56, v28, v37
	v_mov_b32_e32 v41, v54
	v_mov_b32_e32 v54, v53
	v_mov_b32_e32 v40, v52
	v_pk_mul_f32 v[34:35], v[26:27], v[54:55]
	v_pk_mul_f32 v[52:53], v[22:23], v[54:55]
	v_mul_f32_e32 v54, v24, v36
	v_mul_f32_e32 v58, v28, v36
	v_mul_f32_e32 v60, v24, v37
	v_mov_b32_e32 v36, v25
	v_mov_b32_e32 v37, v29
	v_pk_mul_f32 v[36:37], v[36:37], v[38:39]
	v_pk_fma_f32 v[34:35], v[22:23], v[40:41], v[34:35] neg_lo:[0,0,1] neg_hi:[0,0,1]
	v_mov_b32_e32 v55, v36
	v_mov_b32_e32 v57, v37
	v_pk_add_f32 v[36:37], v[54:55], v[56:57] neg_lo:[0,1] neg_hi:[0,1]
	v_mov_b32_e32 v54, v29
	v_mov_b32_e32 v55, v25
	v_pk_mul_f32 v[38:39], v[54:55], v[38:39]
	v_mul_f32_e32 v56, v32, v43
	v_mov_b32_e32 v59, v38
	v_mov_b32_e32 v61, v39
	v_pk_fma_f32 v[38:39], v[26:27], v[40:41], v[52:53]
	v_mov_b32_e32 v53, v48
	v_mov_b32_e32 v48, v47
	v_pk_add_f32 v[40:41], v[58:59], v[60:61]
	v_mov_b32_e32 v52, v46
	v_pk_mul_f32 v[46:47], v[30:31], v[48:49]
	v_pk_mul_f32 v[54:55], v[18:19], v[48:49]
	v_mul_f32_e32 v48, v20, v42
	v_mul_f32_e32 v58, v32, v42
	v_mul_f32_e32 v60, v20, v43
	v_mov_b32_e32 v42, v21
	v_mov_b32_e32 v43, v33
	v_pk_mul_f32 v[42:43], v[42:43], v[44:45]
	v_pk_fma_f32 v[46:47], v[18:19], v[52:53], v[46:47] neg_lo:[0,0,1] neg_hi:[0,0,1]
	v_mov_b32_e32 v49, v42
	v_mov_b32_e32 v57, v43
	v_mov_b32_e32 v42, v33
	v_mov_b32_e32 v43, v21
	v_pk_mul_f32 v[42:43], v[42:43], v[44:45]
	v_pk_add_f32 v[48:49], v[48:49], v[56:57] neg_lo:[0,1] neg_hi:[0,1]
	v_mov_b32_e32 v59, v42
	v_mov_b32_e32 v61, v43
	v_pk_fma_f32 v[42:43], v[30:31], v[52:53], v[54:55]
	v_pk_add_f32 v[44:45], v[58:59], v[60:61]
	s_and_b64 vcc, exec, s[8:9]
	s_mov_b64 s[52:53], -1
	s_cbranch_vccz .LBB0_388

.LBB0_391:
	v_add_u32_e32 v34, 0xb0, v178
	v_mov_b64_e32 v[28:29], v[16:17]
	v_mov_b64_e32 v[24:25], v[12:13]
	v_mov_b64_e32 v[32:33], v[4:5]
	v_mov_b64_e32 v[20:21], v[8:9]
	v_and_b32_e32 v35, 0x7ff, v34
	s_andn2_b64 vcc, exec, s[52:53]
	v_mov_b64_e32 v[26:27], v[14:15]
	v_mov_b64_e32 v[22:23], v[10:11]
	v_mov_b64_e32 v[30:31], v[2:3]
	v_mov_b64_e32 v[18:19], v[6:7]
	s_cbranch_vccnz .LBB0_398
	v_lshlrev_b32_e32 v18, 9, v35
	v_mov_b32_e32 v19, v159
	v_lshl_add_u64 v[18:19], v[168:169], 0, v[18:19]
	s_waitcnt vmcnt(4)
	v_mov_b32_e32 v26, v230
	v_mov_b32_e32 v27, v231
	v_mov_b32_e32 v28, v232
	v_mov_b32_e32 v29, v233
	v_mov_b32_e32 v30, v222
	v_mov_b32_e32 v31, v223
	v_mov_b32_e32 v32, v224
	v_mov_b32_e32 v33, v225
	v_mov_b32_e32 v20, v218
	v_mov_b32_e32 v21, v219
	v_mov_b32_e32 v22, v220
	v_mov_b32_e32 v23, v221
	v_mov_b32_e32 v36, v214
	v_mov_b32_e32 v37, v215
	v_mov_b32_e32 v38, v216
	v_mov_b32_e32 v39, v217
	v_mul_f32_e32 v40, v12, v21
	v_mov_b32_e32 v25, v38
	v_mov_b32_e32 v38, v37
	v_mov_b32_e32 v24, v36
	v_pk_mul_f32 v[18:19], v[10:11], v[38:39]
	v_pk_mul_f32 v[36:37], v[6:7], v[38:39]
	v_mul_f32_e32 v38, v8, v20
	v_mul_f32_e32 v42, v12, v20
	v_mul_f32_e32 v44, v8, v21
	v_mov_b32_e32 v20, v9
	v_mov_b32_e32 v21, v13
	v_pk_mul_f32 v[20:21], v[20:21], v[22:23]
	v_pk_fma_f32 v[18:19], v[6:7], v[24:25], v[18:19] neg_lo:[0,0,1] neg_hi:[0,0,1]
	v_mov_b32_e32 v39, v20
	v_mov_b32_e32 v41, v21
	v_pk_add_f32 v[20:21], v[38:39], v[40:41] neg_lo:[0,1] neg_hi:[0,1]
	v_mov_b32_e32 v38, v13
	v_mov_b32_e32 v39, v9
	v_pk_mul_f32 v[22:23], v[38:39], v[22:23]
	v_mul_f32_e32 v40, v16, v27
	v_mov_b32_e32 v43, v22
	v_mov_b32_e32 v45, v23
	v_pk_fma_f32 v[22:23], v[10:11], v[24:25], v[36:37]
	v_mov_b32_e32 v37, v32
	v_mov_b32_e32 v32, v31
	v_pk_add_f32 v[24:25], v[42:43], v[44:45]
	v_mov_b32_e32 v36, v30
	v_pk_mul_f32 v[30:31], v[14:15], v[32:33]
	v_pk_mul_f32 v[38:39], v[2:3], v[32:33]
	v_mul_f32_e32 v32, v4, v26
	v_mul_f32_e32 v42, v16, v26
	v_mul_f32_e32 v44, v4, v27
	v_mov_b32_e32 v26, v5
	v_mov_b32_e32 v27, v17
	v_pk_mul_f32 v[26:27], v[26:27], v[28:29]
	v_pk_fma_f32 v[30:31], v[2:3], v[36:37], v[30:31] neg_lo:[0,0,1] neg_hi:[0,0,1]
	v_mov_b32_e32 v33, v26
	v_mov_b32_e32 v41, v27
	v_mov_b32_e32 v26, v17
	v_mov_b32_e32 v27, v5
	v_pk_mul_f32 v[26:27], v[26:27], v[28:29]
	v_pk_add_f32 v[32:33], v[32:33], v[40:41] neg_lo:[0,1] neg_hi:[0,1]
	v_mov_b32_e32 v43, v26
	v_mov_b32_e32 v45, v27
	v_pk_fma_f32 v[26:27], v[14:15], v[36:37], v[38:39]
	v_pk_add_f32 v[28:29], v[42:43], v[44:45]
	s_and_b64 vcc, exec, s[8:9]
	s_mov_b64 s[8:9], -1
	s_cbranch_vccz .LBB0_399

	.amdhsa_kernel _Z3fwd6Params
		.amdhsa_group_segment_fixed_size 0
		.amdhsa_private_segment_fixed_size 0
		.amdhsa_kernarg_size 480
		.amdhsa_user_sgpr_count 2
		.amdhsa_user_sgpr_dispatch_ptr 0
		.amdhsa_user_sgpr_queue_ptr 0
		.amdhsa_user_sgpr_kernarg_segment_ptr 1
		.amdhsa_user_sgpr_dispatch_id 0
		.amdhsa_user_sgpr_kernarg_preload_length 0
		.amdhsa_user_sgpr_kernarg_preload_offset 0
		.amdhsa_user_sgpr_private_segment_size 0
		.amdhsa_uses_dynamic_stack 0
		.amdhsa_enable_private_segment 0
		.amdhsa_system_sgpr_workgroup_id_x 1
		.amdhsa_system_sgpr_workgroup_id_y 0
		.amdhsa_system_sgpr_workgroup_id_z 0
		.amdhsa_system_sgpr_workgroup_info 0
		.amdhsa_system_vgpr_workitem_id 0
		.amdhsa_next_free_vgpr 256
		.amdhsa_next_free_sgpr 102
		.amdhsa_accum_offset 256
		.amdhsa_reserve_vcc 1
		.amdhsa_float_round_mode_32 0
		.amdhsa_float_round_mode_16_64 0
		.amdhsa_float_denorm_mode_32 3
		.amdhsa_float_denorm_mode_16_64 3
		.amdhsa_dx10_clamp 1
		.amdhsa_ieee_mode 1
		.amdhsa_fp16_overflow 0
		.amdhsa_tg_split 0
		.amdhsa_exception_fp_ieee_invalid_op 0
		.amdhsa_exception_fp_denorm_src 0
		.amdhsa_exception_fp_ieee_div_zero 0
		.amdhsa_exception_fp_ieee_overflow 0
		.amdhsa_exception_fp_ieee_underflow 0
		.amdhsa_exception_fp_ieee_inexact 0
		.amdhsa_exception_int_div_zero 0
	.end_amdhsa_kernel

amdhsa.kernels:
  - .agpr_count:     0
    .args:
      - .offset:         0
        .size:           224
        .value_kind:     by_value
      - .offset:         224
        .size:           4
        .value_kind:     hidden_block_count_x
      - .offset:         228
        .size:           4
        .value_kind:     hidden_block_count_y
      - .offset:         232
        .size:           4
        .value_kind:     hidden_block_count_z
      - .offset:         236
        .size:           2
        .value_kind:     hidden_group_size_x
      - .offset:         238
        .size:           2
        .value_kind:     hidden_group_size_y
      - .offset:         240
        .size:           2
        .value_kind:     hidden_group_size_z
      - .offset:         242
        .size:           2
        .value_kind:     hidden_remainder_x
      - .offset:         244
        .size:           2
        .value_kind:     hidden_remainder_y
      - .offset:         246
        .size:           2
        .value_kind:     hidden_remainder_z
      - .offset:         264
        .size:           8
        .value_kind:     hidden_global_offset_x
      - .offset:         272
        .size:           8
        .value_kind:     hidden_global_offset_y
      - .offset:         280
        .size:           8
        .value_kind:     hidden_global_offset_z
      - .offset:         288
        .size:           2
        .value_kind:     hidden_grid_dims
      - .offset:         344
        .size:           4
        .value_kind:     hidden_dynamic_lds_size
    .group_segment_fixed_size: 0
    .kernarg_segment_align: 8
    .kernarg_segment_size: 480
    .language:       OpenCL C
    .language_version:
      - 2
      - 0
    .max_flat_workgroup_size: 512
    .name:           _Z3fwd6Params
    .private_segment_fixed_size: 0
    .sgpr_count:     108
    .sgpr_spill_count: 109
    .symbol:         _Z3fwd6Params.kd
    .uniform_work_group_size: 1
    .uses_dynamic_stack: false
    .vgpr_count:     256
    .vgpr_spill_count: 0
    .wavefront_size: 64
